# MLP2 output stores sc1 instead of nt; MLP1 stores sc1 (write-through big streaming outputs)
# speedup vs baseline: 1.0164x; 1.0091x over previous
.LBB6_9:
	s_mul_i32 s22, s58, 0xc0
	v_add_u32_e32 v116, s22, v129
	v_ashrrev_i32_e32 v117, 31, v116
	v_lshlrev_b64 v[124:125], 2, v[116:117]
	v_lshl_add_u64 v[132:133], s[18:19], 0, v[124:125]
	global_load_dwordx4 v[116:119], v[132:133], off
	global_load_dwordx4 v[120:123], v[132:133], off offset:64
	s_nop 0
	global_load_dwordx4 v[132:135], v[132:133], off offset:128
	v_lshl_add_u32 v131, s57, 7, v126
	v_mad_i64_i32 v[136:137], s[22:23], v131, s39, 0
	v_or_b32_e32 v138, 16, v131
	v_or_b32_e32 v140, 32, v131
	v_or_b32_e32 v131, 48, v131
	v_mad_i64_i32 v[138:139], s[22:23], v138, s39, 0
	v_mad_i64_i32 v[140:141], s[22:23], v140, s39, 0
	v_mad_i64_i32 v[142:143], s[22:23], v131, s39, 0
	v_lshl_add_u64 v[136:137], v[136:137], 2, s[8:9]
	v_lshl_add_u64 v[138:139], v[138:139], 2, s[8:9]
	v_lshl_add_u64 v[140:141], v[140:141], 2, s[8:9]
	v_lshl_add_u64 v[142:143], v[142:143], 2, s[8:9]
	v_lshl_add_u64 v[136:137], v[136:137], 0, v[124:125]
	v_lshl_add_u64 v[138:139], v[138:139], 0, v[124:125]
	v_lshl_add_u64 v[140:141], v[140:141], 0, v[124:125]
	v_lshl_add_u64 v[124:125], v[142:143], 0, v[124:125]
	s_mov_b32 s57, s64
	s_mov_b32 s58, s63
	s_mov_b64 s[24:25], s[4:5]
	s_mov_b64 s[22:23], s[26:27]
	s_mov_b64 vcc, s[0:1]
	s_waitcnt vmcnt(0)
	v_pk_add_f32 v[42:43], v[42:43], v[118:119]
	v_pk_add_f32 v[40:41], v[40:41], v[116:117]
	v_pk_add_f32 v[46:47], v[46:47], v[122:123]
	v_pk_add_f32 v[44:45], v[44:45], v[120:121]
	v_pk_add_f32 v[38:39], v[38:39], v[134:135]
	v_pk_add_f32 v[36:37], v[36:37], v[132:133]
	v_pk_add_f32 v[34:35], v[34:35], v[118:119]
	v_pk_add_f32 v[32:33], v[32:33], v[116:117]
	v_pk_add_f32 v[30:31], v[30:31], v[122:123]
	v_pk_add_f32 v[28:29], v[28:29], v[120:121]
	v_pk_add_f32 v[26:27], v[26:27], v[134:135]
	v_pk_add_f32 v[24:25], v[24:25], v[132:133]
	v_pk_add_f32 v[142:143], v[22:23], v[118:119]
	v_pk_add_f32 v[144:145], v[20:21], v[116:117]
	v_pk_add_f32 v[146:147], v[18:19], v[122:123]
	v_pk_add_f32 v[148:149], v[16:17], v[120:121]
	v_pk_add_f32 v[150:151], v[14:15], v[134:135]
	v_pk_add_f32 v[152:153], v[12:13], v[132:133]
	v_pk_add_f32 v[118:119], v[10:11], v[118:119]
	v_pk_add_f32 v[116:117], v[8:9], v[116:117]
	v_pk_add_f32 v[122:123], v[6:7], v[122:123]
	v_pk_add_f32 v[120:121], v[4:5], v[120:121]
	v_pk_add_f32 v[134:135], v[2:3], v[134:135]
	v_pk_add_f32 v[132:133], v[0:1], v[132:133]
	v_pk_add_f32 v[2:3], v[42:43], v[58:59]
	v_pk_add_f32 v[0:1], v[40:41], v[60:61]
	v_pk_add_f32 v[6:7], v[46:47], v[62:63]
	v_pk_add_f32 v[4:5], v[44:45], v[64:65]
	v_pk_add_f32 v[10:11], v[38:39], v[66:67]
	v_pk_add_f32 v[8:9], v[36:37], v[68:69]
	v_pk_add_f32 v[14:15], v[34:35], v[70:71]
	v_pk_add_f32 v[12:13], v[32:33], v[72:73]
	v_pk_add_f32 v[18:19], v[30:31], v[74:75]
	v_pk_add_f32 v[16:17], v[28:29], v[76:77]
	v_pk_add_f32 v[22:23], v[26:27], v[78:79]
	v_pk_add_f32 v[20:21], v[24:25], v[80:81]
	v_pk_add_f32 v[26:27], v[142:143], v[82:83]
	v_pk_add_f32 v[24:25], v[144:145], v[84:85]
	v_pk_add_f32 v[30:31], v[146:147], v[86:87]
	v_pk_add_f32 v[28:29], v[148:149], v[88:89]
	v_pk_add_f32 v[34:35], v[150:151], v[90:91]
	v_pk_add_f32 v[32:33], v[152:153], v[92:93]
	v_pk_add_f32 v[38:39], v[118:119], v[94:95]
	v_pk_add_f32 v[36:37], v[116:117], v[96:97]
	v_pk_add_f32 v[42:43], v[122:123], v[98:99]
	v_pk_add_f32 v[40:41], v[120:121], v[100:101]
	v_pk_add_f32 v[46:47], v[134:135], v[104:105]
	v_pk_add_f32 v[44:45], v[132:133], v[102:103]
	global_store_dwordx4 v[136:137], v[0:3], off sc1
	global_store_dwordx4 v[136:137], v[4:7], off offset:64 sc1
	global_store_dwordx4 v[136:137], v[8:11], off offset:128 sc1
	global_store_dwordx4 v[138:139], v[12:15], off sc1
	global_store_dwordx4 v[138:139], v[16:19], off offset:64 sc1
	global_store_dwordx4 v[138:139], v[20:23], off offset:128 sc1
	global_store_dwordx4 v[140:141], v[24:27], off sc1
	global_store_dwordx4 v[140:141], v[28:31], off offset:64 sc1
	global_store_dwordx4 v[140:141], v[32:35], off offset:128 sc1
	global_store_dwordx4 v[124:125], v[36:39], off sc1
	global_store_dwordx4 v[124:125], v[40:43], off offset:64 sc1
	global_store_dwordx4 v[124:125], v[44:47], off offset:128 sc1
	s_cbranch_vccnz .LBB6_23
